# GEMM bodies: first K-tile of each unit peeled with SrcC=0, accumulator zeroing (128 v_mov per unit) removed; plus wide FFN epilogue stores
# speedup vs baseline: 1.0206x; 1.0042x over previous
; #define G8_GOFF(dst, uord) do { _Pragma("unroll") for (int _h = 0; _h < 2; ++_h) _Pragma("unroll") for (int _i = 0; _i < 2; ++_i) dst[_h][_i] = rtab[((uord) & 7) * 256 + _h * 128 + gR0 + 64 * _i] + gC2; } while (0)
; #define G8_LDA(dst, b, h) do { _Pragma("unroll") for (int m = 0; m < 4; ++m) _Pragma("unroll") for (int k = 0; k < 2; ++k) dst[m][k] = *(const LAS i32x4*)(lds + G8_SA(b, h) + aoff + m * 2048 + k * 1024); } while (0)
; #define G8_LDB(dst, b, h) do { _Pragma("unroll") for (int n = 0; n < 2; ++n) _Pragma("unroll") for (int k = 0; k < 2; ++k) dst[n][k] = *(const LAS i32x4*)(lds + G8_SB(b, h) + boff + n * 2048 + k * 1024); } while (0)
; #define G8_WAIT_V(n) asm volatile("s_waitcnt vmcnt(" #n ")" ::: "memory")
; #define G8_WAIT_L(n) asm volatile("s_waitcnt lgkmcnt(" #n ")" ::: "memory")
; #define G8_BAR __builtin_amdgcn_s_barrier()
; #define G8_SCHED __builtin_amdgcn_sched_barrier(0)
; template <bool FP8>
; __device__ __forceinline__ void gemm_phase(LAS unsigned char* lds, const Desc& prob) {
;     ...
;         const bool has_next = get_tile(prob, ui + 1, nxt);
;         const char* nA = has_next ? nxt.a : cA; const char* nB = has_next ? nxt.b : cB; hAn = has_next ? nxt.h1 : hAc;
;         if (GAT) { G8_GOFF(goffN, has_next ? ui + 1 : ui); }
;         for (int t = 0; t < nt; t += 2) {
;             const bool last = (t == nt - 2);
;             const char* a1 = cA + (size_t)(t + 1) * kstep;
;             const char* a2 = last ? nA : cA + (size_t)(t + 2) * kstep; const char* b2 = last ? nB : cB + (size_t)(t + 2) * kstep;
;             const char* a3 = a2 + kstep; const char* b3 = b2 + kstep;
;             G8_LDB(B0, 0, 0); G8_LDB(B1, 0, 1); G8_SCHED; G8_LDA(At, 0, 0); G8_STGA(G8_SA(1, 1), 1, false, a1, (t + 1) * 128);
;             G8_WAIT_V(8); G8_WAIT_L(0); G8_BAR; G8_MMA(0, 0, At, B0); G8_MMA(0, 1, At, B1); G8_BAR; G8_SCHED;
.LBB0_486:
	s_and_b64 s[6:7], s[96:97], exec
	s_cselect_b32 s2, s31, s17
	s_cselect_b32 s12, s30, s16
	s_cselect_b32 s13, s11, s41
	s_cselect_b32 s20, s10, s40
	s_add_u32 s16, s16, 0x80
	s_addc_u32 s17, s17, 0
	v_ashrrev_i32_e32 v133, 31, v132
	s_add_u32 s21, s40, 0x100
	s_addc_u32 s27, s41, 0
	v_lshl_add_u64 v[134:135], v[190:191], 0, v[132:133]
	v_lshl_add_u64 v[136:137], v[192:193], 0, v[132:133]
	s_mov_b32 s6, 0
	s_add_i32 s37, s6, 2
	s_add_u32 s38, s16, 0x80
	s_addc_u32 s40, s17, 0
	s_cmp_eq_u32 s61, s6
	s_cselect_b64 s[8:9], -1, 0
	s_and_b64 s[6:7], s[8:9], exec
	s_cselect_b32 s7, s2, s40
	s_cselect_b32 s6, s12, s38
	v_add_u32_e32 v66, s33, v1
	s_cselect_b32 s41, s13, s27
	s_cselect_b32 s40, s20, s21
	s_add_i32 s38, 0, 0x14000
	ds_read_b128 v[138:141], v66
	ds_read_b128 v[142:145], v66 offset:1024
	ds_read_b128 v[146:149], v66 offset:2048
	ds_read_b128 v[150:153], v66 offset:3072
	v_add_u32_e32 v66, s38, v1
	ds_read_b128 v[154:157], v66
	ds_read_b128 v[158:161], v66 offset:1024
	ds_read_b128 v[162:165], v66 offset:2048
	ds_read_b128 v[166:169], v66 offset:3072
	v_lshl_add_u64 v[178:179], s[16:17], 0, v[134:135]
	s_add_i32 m0, s89, 0xc000
	ds_read_b128 v[170:173], v220
	ds_read_b128 v[174:177], v220 offset:1024
	ds_read_b128 v[198:201], v220 offset:2048
	ds_read_b128 v[202:205], v220 offset:3072
	ds_read_b128 v[206:209], v220 offset:4096
	ds_read_b128 v[210:213], v220 offset:5120
	ds_read_b128 v[214:217], v220 offset:6144
	ds_read_b128 v[222:225], v220 offset:7168
	global_load_lds_dwordx4 v[178:179], off
	v_lshl_add_u64 v[178:179], s[16:17], 0, v[136:137]
	s_add_i32 m0, s89, 0xe000
	s_nop 0
	global_load_lds_dwordx4 v[178:179], off
	s_waitcnt vmcnt(8)
	s_waitcnt lgkmcnt(0)
	s_barrier
	s_setprio 1
	s_waitcnt lgkmcnt(0)
	v_mfma_f32_16x16x32_bf16 v[128:131], v[138:141], v[170:173], 0
	v_mfma_f32_16x16x32_bf16 v[124:127], v[146:149], v[170:173], 0
	v_mfma_f32_16x16x32_bf16 v[112:115], v[138:141], v[198:201], 0
	v_mfma_f32_16x16x32_bf16 v[108:111], v[146:149], v[198:201], 0
	v_mfma_f32_16x16x32_bf16 v[96:99], v[138:141], v[206:209], 0
	v_mfma_f32_16x16x32_bf16 v[92:95], v[146:149], v[206:209], 0
	v_mfma_f32_16x16x32_bf16 v[80:83], v[138:141], v[214:217], 0
	v_mfma_f32_16x16x32_bf16 v[76:79], v[146:149], v[214:217], 0
	v_mfma_f32_16x16x32_bf16 v[128:131], v[142:145], v[174:177], v[128:131]
	v_mfma_f32_16x16x32_bf16 v[124:127], v[150:153], v[174:177], v[124:127]
	v_mfma_f32_16x16x32_bf16 v[112:115], v[142:145], v[202:205], v[112:115]
	v_mfma_f32_16x16x32_bf16 v[108:111], v[150:153], v[202:205], v[108:111]
	v_mfma_f32_16x16x32_bf16 v[96:99], v[142:145], v[210:213], v[96:99]
	v_mfma_f32_16x16x32_bf16 v[92:95], v[150:153], v[210:213], v[92:95]
	v_mfma_f32_16x16x32_bf16 v[80:83], v[142:145], v[222:225], v[80:83]
	v_mfma_f32_16x16x32_bf16 v[76:79], v[150:153], v[222:225], v[76:79]
	s_setprio 0
	s_setprio 1
	v_mfma_f32_16x16x32_bf16 v[120:123], v[154:157], v[170:173], 0
	v_mfma_f32_16x16x32_bf16 v[116:119], v[162:165], v[170:173], 0
	v_mfma_f32_16x16x32_bf16 v[104:107], v[154:157], v[198:201], 0
	v_mfma_f32_16x16x32_bf16 v[100:103], v[162:165], v[198:201], 0
	v_mfma_f32_16x16x32_bf16 v[88:91], v[154:157], v[206:209], 0
	v_mfma_f32_16x16x32_bf16 v[84:87], v[162:165], v[206:209], 0
	v_mfma_f32_16x16x32_bf16 v[72:75], v[154:157], v[214:217], 0
	v_mfma_f32_16x16x32_bf16 v[68:71], v[162:165], v[214:217], 0
	v_mfma_f32_16x16x32_bf16 v[120:123], v[158:161], v[174:177], v[120:123]
	v_mfma_f32_16x16x32_bf16 v[116:119], v[166:169], v[174:177], v[116:119]
	v_mfma_f32_16x16x32_bf16 v[104:107], v[158:161], v[202:205], v[104:107]
	v_mfma_f32_16x16x32_bf16 v[100:103], v[166:169], v[202:205], v[100:103]
	v_mfma_f32_16x16x32_bf16 v[88:91], v[158:161], v[210:213], v[88:91]
	v_mfma_f32_16x16x32_bf16 v[84:87], v[166:169], v[210:213], v[84:87]
	v_mfma_f32_16x16x32_bf16 v[72:75], v[158:161], v[222:225], v[72:75]
	v_mfma_f32_16x16x32_bf16 v[68:71], v[166:169], v[222:225], v[68:71]
	s_setprio 0
	s_barrier
; #define G8_STAGE(bufoff, gbase, voff) do { _Pragma("unroll") for (int _i = 0; _i < 2; ++_i) \
;         __builtin_amdgcn_global_load_lds((const unsigned*)((const char*)(gbase) + (voff)[_i]), (LAS unsigned*)(lds + (bufoff) + ldsw + _i * 8192), 16, 0, 0); } while (0)
; #define G8_LDA(dst, b, h) do { _Pragma("unroll") for (int m = 0; m < 4; ++m) _Pragma("unroll") for (int k = 0; k < 2; ++k) dst[m][k] = *(const LAS i32x4*)(lds + G8_SA(b, h) + aoff + m * 2048 + k * 1024); } while (0)
; #define G8_WAIT_V(n) asm volatile("s_waitcnt vmcnt(" #n ")" ::: "memory")
; #define G8_WAIT_L(n) asm volatile("s_waitcnt lgkmcnt(" #n ")" ::: "memory")
; #define G8_BAR __builtin_amdgcn_s_barrier()
; #define G8_SCHED __builtin_amdgcn_sched_barrier(0)
; template <bool FP8>
; __device__ __forceinline__ void gemm_phase(LAS unsigned char* lds, const Desc& prob) {
;     ...
;             G8_LDA(At, 0, 1); G8_STAGE(G8_SB(0, 0), b2, voffB); G8_STAGE(G8_SB(0, 1), b2 + hstepB, voffB); G8_STGA(G8_SA(0, 0), 0, last, a2, last ? 0 : (t + 2) * 128);
;             G8_WAIT_V(8); G8_WAIT_L(0); G8_BAR; G8_MMA(1, 0, At, B0); G8_MMA(1, 1, At, B1); G8_BAR; G8_SCHED;
	s_add_i32 s42, s33, s59
	v_lshl_add_u64 v[178:179], s[40:41], 0, v[182:183]
	s_mov_b32 m0, s42
	ds_read_b128 v[170:173], v220 offset:16384
	ds_read_b128 v[174:177], v220 offset:17408
	ds_read_b128 v[198:201], v220 offset:18432
	ds_read_b128 v[202:205], v220 offset:19456
	ds_read_b128 v[206:209], v220 offset:20480
	ds_read_b128 v[210:213], v220 offset:21504
	ds_read_b128 v[214:217], v220 offset:22528
	ds_read_b128 v[222:225], v220 offset:23552
	global_load_lds_dwordx4 v[178:179], off
	s_add_i32 m0, s42, 0x2000
	v_lshl_add_u64 v[194:195], s[40:41], 0, v[186:187]
	s_add_u32 s40, s40, s68
	s_addc_u32 s41, s41, s69
	s_add_i32 s38, s38, s59
	global_load_lds_dwordx4 v[194:195], off
	v_lshl_add_u64 v[226:227], s[40:41], 0, v[182:183]
	s_mov_b32 m0, s38
	v_lshl_add_u64 v[228:229], s[40:41], 0, v[186:187]
	global_load_lds_dwordx4 v[226:227], off
	s_add_i32 m0, s38, 0x2000
	v_lshl_add_u64 v[230:231], s[6:7], 0, v[180:181]
	global_load_lds_dwordx4 v[228:229], off
	s_mov_b32 m0, s89
	v_lshl_add_u64 v[232:233], s[6:7], 0, v[184:185]
	global_load_lds_dwordx4 v[230:231], off
	s_mov_b32 m0, s94
	s_nop 0
	global_load_lds_dwordx4 v[232:233], off
	s_waitcnt vmcnt(8)
	s_waitcnt lgkmcnt(0)
	s_barrier
	s_setprio 1
	s_waitcnt lgkmcnt(0)
	v_mfma_f32_16x16x32_bf16 v[62:65], v[138:141], v[170:173], 0
	v_mfma_f32_16x16x32_bf16 v[58:61], v[146:149], v[170:173], 0
	v_mfma_f32_16x16x32_bf16 v[46:49], v[138:141], v[198:201], 0
	v_mfma_f32_16x16x32_bf16 v[42:45], v[146:149], v[198:201], 0
	v_mfma_f32_16x16x32_bf16 v[30:33], v[138:141], v[206:209], 0
	v_mfma_f32_16x16x32_bf16 v[26:29], v[146:149], v[206:209], 0
	v_mfma_f32_16x16x32_bf16 v[14:17], v[138:141], v[214:217], 0
	v_mfma_f32_16x16x32_bf16 v[10:13], v[146:149], v[214:217], 0
	v_mfma_f32_16x16x32_bf16 v[62:65], v[142:145], v[174:177], v[62:65]
	v_mfma_f32_16x16x32_bf16 v[58:61], v[150:153], v[174:177], v[58:61]
	v_mfma_f32_16x16x32_bf16 v[46:49], v[142:145], v[202:205], v[46:49]
	v_mfma_f32_16x16x32_bf16 v[42:45], v[150:153], v[202:205], v[42:45]
	v_mfma_f32_16x16x32_bf16 v[30:33], v[142:145], v[210:213], v[30:33]
	v_mfma_f32_16x16x32_bf16 v[26:29], v[150:153], v[210:213], v[26:29]
	v_mfma_f32_16x16x32_bf16 v[14:17], v[142:145], v[222:225], v[14:17]
	v_mfma_f32_16x16x32_bf16 v[10:13], v[150:153], v[222:225], v[10:13]
	s_setprio 0
	s_setprio 1
	v_mfma_f32_16x16x32_bf16 v[54:57], v[154:157], v[170:173], 0
	v_mfma_f32_16x16x32_bf16 v[50:53], v[162:165], v[170:173], 0
	v_mfma_f32_16x16x32_bf16 v[38:41], v[154:157], v[198:201], 0
	v_mfma_f32_16x16x32_bf16 v[34:37], v[162:165], v[198:201], 0
	v_mfma_f32_16x16x32_bf16 v[22:25], v[154:157], v[206:209], 0
	v_mfma_f32_16x16x32_bf16 v[18:21], v[162:165], v[206:209], 0
	v_mfma_f32_16x16x32_bf16 v[6:9], v[154:157], v[214:217], 0
	v_mfma_f32_16x16x32_bf16 v[2:5], v[162:165], v[214:217], 0
	v_mfma_f32_16x16x32_bf16 v[54:57], v[158:161], v[174:177], v[54:57]
	v_mfma_f32_16x16x32_bf16 v[50:53], v[166:169], v[174:177], v[50:53]
	v_mfma_f32_16x16x32_bf16 v[38:41], v[158:161], v[202:205], v[38:41]
	v_mfma_f32_16x16x32_bf16 v[34:37], v[166:169], v[202:205], v[34:37]
	v_mfma_f32_16x16x32_bf16 v[22:25], v[158:161], v[210:213], v[22:25]
	v_mfma_f32_16x16x32_bf16 v[18:21], v[166:169], v[210:213], v[18:21]
	v_mfma_f32_16x16x32_bf16 v[6:9], v[158:161], v[222:225], v[6:9]
	v_mfma_f32_16x16x32_bf16 v[2:5], v[166:169], v[222:225], v[2:5]
	s_setprio 0
	s_barrier
	s_branch .Lbfz_mid

; #define G8_LDA(dst, b, h) do { _Pragma("unroll") for (int m = 0; m < 4; ++m) _Pragma("unroll") for (int k = 0; k < 2; ++k) dst[m][k] = *(const LAS i32x4*)(lds + G8_SA(b, h) + aoff + m * 2048 + k * 1024); } while (0)
; #define G8_LDB(dst, b, h) do { _Pragma("unroll") for (int n = 0; n < 2; ++n) _Pragma("unroll") for (int k = 0; k < 2; ++k) dst[n][k] = *(const LAS i32x4*)(lds + G8_SB(b, h) + boff + n * 2048 + k * 1024); } while (0)
; #define G8_WAIT_V(n) asm volatile("s_waitcnt vmcnt(" #n ")" ::: "memory")
; #define G8_WAIT_L(n) asm volatile("s_waitcnt lgkmcnt(" #n ")" ::: "memory")
; #define G8_BAR __builtin_amdgcn_s_barrier()
; #define G8_SCHED __builtin_amdgcn_sched_barrier(0)
; template <bool FP8>
; __device__ __forceinline__ void gemm_phase(LAS unsigned char* lds, const Desc& prob) {
;     ...
;             G8_LDB(B0, 1, 0); G8_LDB(B1, 1, 1); G8_SCHED; G8_LDA(At, 1, 0); G8_STGA(G8_SA(0, 1), 1, last, a2, last ? 0 : (t + 2) * 128);
;             G8_WAIT_V(8); G8_WAIT_L(0); G8_BAR; G8_MMA(0, 0, At, B0); G8_MMA(0, 1, At, B1); G8_BAR; G8_SCHED;
.Lbfz_mid:
	s_add_i32 s38, 0, 0x18000
	v_add_u32_e32 v66, s38, v1
	s_add_i32 s40, 0, 0x1c000
	ds_read_b128 v[138:141], v66
	ds_read_b128 v[142:145], v66 offset:1024
	ds_read_b128 v[146:149], v66 offset:2048
	ds_read_b128 v[150:153], v66 offset:3072
	v_add_u32_e32 v66, s40, v1
	ds_read_b128 v[154:157], v66
	ds_read_b128 v[158:161], v66 offset:1024
	ds_read_b128 v[162:165], v66 offset:2048
	ds_read_b128 v[166:169], v66 offset:3072
	s_and_b64 vcc, s[96:97], s[8:9]
	v_cndmask_b32_e32 v234, v132, v221, vcc
	v_ashrrev_i32_e32 v235, 31, v234
	v_lshl_add_u64 v[234:235], s[6:7], 0, v[234:235]
	s_mov_b32 m0, s95
	v_lshl_add_u64 v[242:243], v[234:235], 0, v[180:181]
	ds_read_b128 v[170:173], v220 offset:32768
	ds_read_b128 v[174:177], v220 offset:33792
	ds_read_b128 v[198:201], v220 offset:34816
	ds_read_b128 v[202:205], v220 offset:35840
	ds_read_b128 v[206:209], v220 offset:36864
	ds_read_b128 v[210:213], v220 offset:37888
	ds_read_b128 v[214:217], v220 offset:38912
	ds_read_b128 v[222:225], v220 offset:39936
	global_load_lds_dwordx4 v[242:243], off
	v_lshl_add_u64 v[234:235], v[234:235], 0, v[184:185]
	s_mov_b32 m0, s64
	s_nop 0
	global_load_lds_dwordx4 v[234:235], off
	s_waitcnt vmcnt(8)
	s_waitcnt lgkmcnt(0)
	s_barrier
	s_setprio 1
	s_waitcnt lgkmcnt(0)
	v_mfma_f32_16x16x32_bf16 v[128:131], v[138:141], v[170:173], v[128:131]
	v_mfma_f32_16x16x32_bf16 v[124:127], v[146:149], v[170:173], v[124:127]
	v_mfma_f32_16x16x32_bf16 v[112:115], v[138:141], v[198:201], v[112:115]
	v_mfma_f32_16x16x32_bf16 v[108:111], v[146:149], v[198:201], v[108:111]
	v_mfma_f32_16x16x32_bf16 v[96:99], v[138:141], v[206:209], v[96:99]
	v_mfma_f32_16x16x32_bf16 v[92:95], v[146:149], v[206:209], v[92:95]
	v_mfma_f32_16x16x32_bf16 v[80:83], v[138:141], v[214:217], v[80:83]
	v_mfma_f32_16x16x32_bf16 v[76:79], v[146:149], v[214:217], v[76:79]
	v_mfma_f32_16x16x32_bf16 v[128:131], v[142:145], v[174:177], v[128:131]
	v_mfma_f32_16x16x32_bf16 v[124:127], v[150:153], v[174:177], v[124:127]
	v_mfma_f32_16x16x32_bf16 v[112:115], v[142:145], v[202:205], v[112:115]
	v_mfma_f32_16x16x32_bf16 v[108:111], v[150:153], v[202:205], v[108:111]
	v_mfma_f32_16x16x32_bf16 v[96:99], v[142:145], v[210:213], v[96:99]
	v_mfma_f32_16x16x32_bf16 v[92:95], v[150:153], v[210:213], v[92:95]
	v_mfma_f32_16x16x32_bf16 v[80:83], v[142:145], v[222:225], v[80:83]
	v_mfma_f32_16x16x32_bf16 v[76:79], v[150:153], v[222:225], v[76:79]
	s_setprio 0
	s_setprio 1
	v_mfma_f32_16x16x32_bf16 v[120:123], v[154:157], v[170:173], v[120:123]
	v_mfma_f32_16x16x32_bf16 v[116:119], v[162:165], v[170:173], v[116:119]
	v_mfma_f32_16x16x32_bf16 v[104:107], v[154:157], v[198:201], v[104:107]
	v_mfma_f32_16x16x32_bf16 v[100:103], v[162:165], v[198:201], v[100:103]
	v_mfma_f32_16x16x32_bf16 v[88:91], v[154:157], v[206:209], v[88:91]
	v_mfma_f32_16x16x32_bf16 v[84:87], v[162:165], v[206:209], v[84:87]
	v_mfma_f32_16x16x32_bf16 v[72:75], v[154:157], v[214:217], v[72:75]
	v_mfma_f32_16x16x32_bf16 v[68:71], v[162:165], v[214:217], v[68:71]
	v_mfma_f32_16x16x32_bf16 v[120:123], v[158:161], v[174:177], v[120:123]
	v_mfma_f32_16x16x32_bf16 v[116:119], v[166:169], v[174:177], v[116:119]
	v_mfma_f32_16x16x32_bf16 v[104:107], v[158:161], v[202:205], v[104:107]
	v_mfma_f32_16x16x32_bf16 v[100:103], v[166:169], v[202:205], v[100:103]
	v_mfma_f32_16x16x32_bf16 v[88:91], v[158:161], v[210:213], v[88:91]
	v_mfma_f32_16x16x32_bf16 v[84:87], v[166:169], v[210:213], v[84:87]
	v_mfma_f32_16x16x32_bf16 v[72:75], v[158:161], v[222:225], v[72:75]
	v_mfma_f32_16x16x32_bf16 v[68:71], v[166:169], v[222:225], v[68:71]
	s_setprio 0
	s_barrier
; #define G8_STAGE(bufoff, gbase, voff) do { _Pragma("unroll") for (int _i = 0; _i < 2; ++_i) \
;         __builtin_amdgcn_global_load_lds((const unsigned*)((const char*)(gbase) + (voff)[_i]), (LAS unsigned*)(lds + (bufoff) + ldsw + _i * 8192), 16, 0, 0); } while (0)
; #define G8_LDA(dst, b, h) do { _Pragma("unroll") for (int m = 0; m < 4; ++m) _Pragma("unroll") for (int k = 0; k < 2; ++k) dst[m][k] = *(const LAS i32x4*)(lds + G8_SA(b, h) + aoff + m * 2048 + k * 1024); } while (0)
; #define G8_WAIT_V(n) asm volatile("s_waitcnt vmcnt(" #n ")" ::: "memory")
; #define G8_WAIT_L(n) asm volatile("s_waitcnt lgkmcnt(" #n ")" ::: "memory")
; #define G8_BAR __builtin_amdgcn_s_barrier()
; #define G8_SCHED __builtin_amdgcn_sched_barrier(0)
; template <bool FP8>
; __device__ __forceinline__ void gemm_phase(LAS unsigned char* lds, const Desc& prob) {
;     ...
;             G8_LDA(At, 1, 1); G8_STAGE(G8_SB(1, 0), b3, voffB); G8_STAGE(G8_SB(1, 1), b3 + hstepB, voffB); G8_STGA(G8_SA(1, 0), 0, last, a3, last ? 128 : (t + 3) * 128);
;             G8_WAIT_V(8); G8_WAIT_L(0); G8_BAR; G8_MMA(1, 0, At, B0); G8_MMA(1, 1, At, B1); G8_BAR; G8_SCHED;
;         }
;         if (wr == 0) G8_BAR;
	s_add_i32 s6, s38, s59
	v_lshl_add_u64 v[178:179], v[178:179], 0, s[22:23]
	s_mov_b32 m0, s6
	ds_read_b128 v[170:173], v220 offset:49152
	ds_read_b128 v[174:177], v220 offset:50176
	ds_read_b128 v[198:201], v220 offset:51200
	ds_read_b128 v[202:205], v220 offset:52224
	ds_read_b128 v[206:209], v220 offset:53248
	ds_read_b128 v[210:213], v220 offset:54272
	ds_read_b128 v[214:217], v220 offset:55296
	ds_read_b128 v[222:225], v220 offset:56320
	global_load_lds_dwordx4 v[178:179], off
	v_lshl_add_u64 v[178:179], v[194:195], 0, s[22:23]
	s_add_i32 m0, s6, 0x2000
	s_add_i32 s6, s40, s59
	global_load_lds_dwordx4 v[178:179], off
	v_lshl_add_u64 v[178:179], v[226:227], 0, s[22:23]
	s_mov_b32 m0, s6
	s_nop 0
	global_load_lds_dwordx4 v[178:179], off
	v_lshl_add_u64 v[178:179], v[228:229], 0, s[22:23]
	s_add_i32 m0, s6, 0x2000
	s_nop 0
	global_load_lds_dwordx4 v[178:179], off
	v_lshl_add_u64 v[178:179], v[230:231], 0, s[22:23]
	s_mov_b32 m0, s24
	s_nop 0
	global_load_lds_dwordx4 v[178:179], off
	v_lshl_add_u64 v[178:179], v[232:233], 0, s[22:23]
	s_mov_b32 m0, s60
	s_nop 0
	global_load_lds_dwordx4 v[178:179], off
	s_waitcnt vmcnt(8)
	s_waitcnt lgkmcnt(0)
	s_barrier
	s_setprio 1
	s_waitcnt lgkmcnt(0)
	v_mfma_f32_16x16x32_bf16 v[62:65], v[138:141], v[170:173], v[62:65]
	v_mfma_f32_16x16x32_bf16 v[58:61], v[146:149], v[170:173], v[58:61]
	v_mfma_f32_16x16x32_bf16 v[46:49], v[138:141], v[198:201], v[46:49]
	v_mfma_f32_16x16x32_bf16 v[42:45], v[146:149], v[198:201], v[42:45]
	v_mfma_f32_16x16x32_bf16 v[30:33], v[138:141], v[206:209], v[30:33]
	v_mfma_f32_16x16x32_bf16 v[26:29], v[146:149], v[206:209], v[26:29]
	v_mfma_f32_16x16x32_bf16 v[14:17], v[138:141], v[214:217], v[14:17]
	v_mfma_f32_16x16x32_bf16 v[10:13], v[146:149], v[214:217], v[10:13]
	v_mfma_f32_16x16x32_bf16 v[62:65], v[142:145], v[174:177], v[62:65]
	v_mfma_f32_16x16x32_bf16 v[58:61], v[150:153], v[174:177], v[58:61]
	v_mfma_f32_16x16x32_bf16 v[46:49], v[142:145], v[202:205], v[46:49]
	v_mfma_f32_16x16x32_bf16 v[42:45], v[150:153], v[202:205], v[42:45]
	v_mfma_f32_16x16x32_bf16 v[30:33], v[142:145], v[210:213], v[30:33]
	v_mfma_f32_16x16x32_bf16 v[26:29], v[150:153], v[210:213], v[26:29]
	v_mfma_f32_16x16x32_bf16 v[14:17], v[142:145], v[222:225], v[14:17]
	v_mfma_f32_16x16x32_bf16 v[10:13], v[150:153], v[222:225], v[10:13]
	s_setprio 0
	s_setprio 1
	v_mfma_f32_16x16x32_bf16 v[54:57], v[154:157], v[170:173], v[54:57]
	v_mfma_f32_16x16x32_bf16 v[50:53], v[162:165], v[170:173], v[50:53]
	v_mfma_f32_16x16x32_bf16 v[38:41], v[154:157], v[198:201], v[38:41]
	v_mfma_f32_16x16x32_bf16 v[34:37], v[162:165], v[198:201], v[34:37]
	v_mfma_f32_16x16x32_bf16 v[22:25], v[154:157], v[206:209], v[22:25]
	v_mfma_f32_16x16x32_bf16 v[18:21], v[162:165], v[206:209], v[18:21]
	v_mfma_f32_16x16x32_bf16 v[6:9], v[154:157], v[214:217], v[6:9]
	v_mfma_f32_16x16x32_bf16 v[2:5], v[162:165], v[214:217], v[2:5]
	v_mfma_f32_16x16x32_bf16 v[54:57], v[158:161], v[174:177], v[54:57]
	v_mfma_f32_16x16x32_bf16 v[50:53], v[166:169], v[174:177], v[50:53]
	v_mfma_f32_16x16x32_bf16 v[38:41], v[158:161], v[202:205], v[38:41]
	v_mfma_f32_16x16x32_bf16 v[34:37], v[166:169], v[202:205], v[34:37]
	v_mfma_f32_16x16x32_bf16 v[22:25], v[158:161], v[210:213], v[22:25]
	v_mfma_f32_16x16x32_bf16 v[18:21], v[166:169], v[210:213], v[18:21]
	v_mfma_f32_16x16x32_bf16 v[6:9], v[158:161], v[222:225], v[6:9]
	v_mfma_f32_16x16x32_bf16 v[2:5], v[166:169], v[222:225], v[2:5]
	s_setprio 0
	s_barrier
	s_add_u32 s16, s16, 0x100
	s_addc_u32 s17, s17, 0
	s_add_u32 s21, s21, 0x100
	s_addc_u32 s27, s27, 0
	s_cmp_ge_u32 s37, s65
	s_mov_b32 s6, s37
	s_cbranch_scc0 .LBB0_487
	s_and_b64 vcc, exec, s[78:79]
	s_cbranch_vccz .LBB0_490
	s_barrier

; #define LAS __attribute__((address_space(3)))
; #define G8_BAR __builtin_amdgcn_s_barrier()
; template <bool FP8>
; __device__ __forceinline__ void gemm_phase(LAS unsigned char* lds, const Desc& prob) {
;     ...
;     const int wid = __builtin_amdgcn_readfirstlane(tid >> 6), lane = tid & 63, wr = wid >> 2, wc = wid & 3, fr = lane & 15, fq = lane >> 4;
;     const int esz = FP8 ? 1 : 2;
;     const int nt = prob.K * esz / 128;
;     int sc_w = prob.sc_w, sc_a = prob.sc_a; asm volatile("" : "+v"(sc_w), "+v"(sc_a));
;     unsigned voffA[2], voffB[2];
; #pragma unroll
;     for (int i = 0; i < 2; ++i) { int R, C; stage_rc(tid * 16 + i * 8192, R, C); const int Rb = (R & ~31) + perm32(R & 31);
;         voffA[i] = (unsigned)(R * prob.lda * esz + C * 2); voffB[i] = (unsigned)(Rb * prob.ldb * esz + C * 2); }
;     const size_t kstep = 128;
;     const size_t hstepB = (size_t)HALF * prob.ldb * esz;
;     const unsigned ldsw = (unsigned)wid * 1024u;
;     const int aoff = lds_byte(wr * 64 + fr, fq * 8), boff = lds_byte(wc * 32 + fr, fq * 8);
;     LAS unsigned* const rtab = (LAS unsigned*)(lds + STAGE_BYTES + 1024);
;     unsigned goffC[2][2] = {{0u, 0u}, {0u, 0u}}, goffN[2][2] = {{0u, 0u}, {0u, 0u}}; int gR0 = 0; unsigned gC2 = 0u;
;     ...
;         if (FP8 && has_next && prob.kind != K_PLE) {
;             const char* nb = nxt.b + (size_t)((cur.pm & 7) * 32) * prob.ldb;
;             __builtin_amdgcn_global_load_lds((const unsigned*)(nb + (size_t)tid * 128), (LAS unsigned*)(lds + 141312 + wid * 256), 4, 0, 0);
;         }
;         if (FP8) asm volatile("s_nop 15\n\ts_nop 15" ::: "memory");
;         epilogue<FP8>(prob, acc, cur, lds);
;         if (!has_next) break;
; #pragma unroll
;         for (int a = 0; a < 2; ++a)
; #pragma unroll
;             for (int b = 0; b < 2; ++b)
; #pragma unroll
;                 for (int m = 0; m < 4; ++m)
; #pragma unroll
;                     for (int n = 0; n < 2; ++n) acc[a][b][m][n] = (f32x4){0.f, 0.f, 0.f, 0.f};
;         cur = nxt; cA = nA; cB = nB; hAc = hAn; ++ui;
;         if (GAT) {
; #pragma unroll
;             for (int _h = 0; _h < 2; ++_h)
; #pragma unroll
;                 for (int _i = 0; _i < 2; ++_i) goffC[_h][_i] = goffN[_h][_i]; }
;         if (wr == 1) G8_BAR;
.LBB0_709:
	s_add_i32 s89, s0, 0xa000
	s_mov_b32 m0, s89
	s_add_i32 s92, s0, 0x1c000
	global_load_lds_dwordx4 v12, s[8:9]
	v_lshl_add_u64 v[6:7], v[6:7], 0, s[22:23]
	s_mov_b32 m0, s92
	s_add_i32 s93, s0, 0x1e000
	global_load_lds_dwordx4 v[6:7], off
	v_lshl_add_u64 v[4:5], v[4:5], 0, s[22:23]
	s_mov_b32 m0, s93
	v_and_b32_e32 v13, 15, v2
	global_load_lds_dwordx4 v[4:5], off
	s_and_b32 s6, 0xffff, s80
	v_and_b32_e32 v14, 48, v2
	v_lshlrev_b32_e32 v13, 6, v13
	v_lshlrev_b32_e32 v16, 2, v2
	s_lshr_b32 s88, s6, 7
	v_or_b32_e32 v15, v13, v14
	s_lshl_b32 s6, s20, 13
	v_and_b32_e32 v16, 32, v16
	v_bitop3_b32 v13, v13, v16, v14 bitop3:0x36
	v_bitop3_b32 v14, v15, s6, v16 bitop3:0xde
	s_lshl_b32 s6, s2, 12
	s_and_b32 s6, s6, 0x3000
	s_add_i32 s94, s88, -2
	s_cmpk_lt_u32 s24, 0x100
	s_cselect_b64 s[68:69], -1, 0
	s_lshl_b32 s2, s2, 8
	s_ashr_i32 s95, s29, 31
	v_or_b32_e32 v13, s6, v13
	v_readlane_b32 s6, v254, 56
	s_cmp_gt_i32 s29, -1
	s_cselect_b64 s[70:71], -1, 0
	v_lshl_add_u32 v251, v8, 2, s6
	s_lshr_b32 s6, s30, 3
	v_writelane_b32 v255, s6, 7
	s_lshr_b32 s6, s25, 2
	v_readlane_b32 s7, v255, 4
	v_lshlrev_b64 v[214:215], 7, v[2:3]
	s_lshl_b32 s97, s25, 3
	s_lshr_b32 s7, s7, 6
	v_mov_b32_e32 v2, s6
	v_mul_u32_u24_e32 v198, s7, v2
	v_cvt_f32_u32_e32 v2, s97
	s_lshr_b32 s7, s25, 3
	v_writelane_b32 v255, s7, 10
	s_lshl_b32 s7, s29, 5
	v_rcp_iflag_f32_e32 v2, v2
	s_and_b32 s7, s7, 0xe0
	s_ashr_i32 s8, s29, 3
	s_add_i32 s7, s7, s8
	v_mul_f32_e32 v2, 0x4f7ffffe, v2
	v_cvt_u32_f32_e32 v2, v2
	s_ashr_i32 s7, s7, 2
	v_writelane_b32 v255, s7, 9
	s_and_b32 s7, s8, 3
	v_writelane_b32 v255, s7, 13
	s_add_i32 s6, s6, -1
	v_writelane_b32 v255, s6, 14
	s_sub_i32 s6, 0, s97
	v_readfirstlane_b32 s7, v2
	s_mul_i32 s6, s6, s7
	s_waitcnt vmcnt(6)
	v_mov_b32_e32 v3, s28
	s_mul_hi_u32 s6, s7, s6
	v_and_b32_e32 v2, 1, v9
	v_mul_u32_u24_e32 v199, s26, v3
	s_add_i32 s6, s7, s6
	v_lshlrev_b32_e32 v2, 6, v2
	v_lshlrev_b32_e32 v3, 1, v10
	s_add_i32 s96, s2, 0
	v_mov_b32_e32 v203, v67
	s_mov_b32 s31, s3
	v_writelane_b32 v255, s6, 15
	v_add3_u32 v216, v11, v2, v3
	v_mov_b32_e32 v217, v67
	v_mov_b32_e32 v249, 0
	s_mov_b32 s27, 0
	s_add_i32 s96, s96, 0x22800
	v_add_u32_e32 v237, 0, v13
	v_add_u32_e32 v250, 0, v14
	v_mov_b32_e32 v239, 0
	v_mov_b32_e32 v252, 0
	v_mov_b32_e32 v241, 0
	s_lshl_b32 s6, s36, 5
	s_and_b32 s6, s6, 0xe0
	v_mov_b32_e32 v2, s58
	v_mul_u32_u24_e32 v66, s6, v2
	v_lshl_add_u64 v[2:3], s[16:17], 0, v[66:67]
	v_lshl_add_u64 v[2:3], v[2:3], 0, v[214:215]
	s_mov_b32 m0, s96
	s_nop 0
	global_load_lds_dword v[2:3], off
	s_barrier
	s_branch .LBB0_711
.LBB0_710:
	s_mov_b64 s[64:65], s[76:77]
	s_mov_b64 s[16:17], s[78:79]
	v_mov_b32_e32 v212, v242
	s_mov_b32 s36, s72
	s_mov_b32 s44, s74
	s_andn2_b64 vcc, exec, s[80:81]
	s_mov_b32 s27, s38
	s_cbranch_vccz .LBB0_809

; #define G8_GOFF(dst, uord) do { _Pragma("unroll") for (int _h = 0; _h < 2; ++_h) _Pragma("unroll") for (int _i = 0; _i < 2; ++_i) dst[_h][_i] = rtab[((uord) & 7) * 256 + _h * 128 + gR0 + 64 * _i] + gC2; } while (0)
; #define G8_LDA(dst, b, h) do { _Pragma("unroll") for (int m = 0; m < 4; ++m) _Pragma("unroll") for (int k = 0; k < 2; ++k) dst[m][k] = *(const LAS i32x4*)(lds + G8_SA(b, h) + aoff + m * 2048 + k * 1024); } while (0)
; #define G8_LDB(dst, b, h) do { _Pragma("unroll") for (int n = 0; n < 2; ++n) _Pragma("unroll") for (int k = 0; k < 2; ++k) dst[n][k] = *(const LAS i32x4*)(lds + G8_SB(b, h) + boff + n * 2048 + k * 1024); } while (0)
; #define G8_SCHED __builtin_amdgcn_sched_barrier(0)
; template <bool FP8>
; __device__ __forceinline__ void gemm_phase(LAS unsigned char* lds, const Desc& prob) {
;     ...
;         const bool has_next = get_tile(prob, ui + 1, nxt);
;         const char* nA = has_next ? nxt.a : cA; const char* nB = has_next ? nxt.b : cB; hAn = has_next ? nxt.h1 : hAc;
;         if (GAT) { G8_GOFF(goffN, has_next ? ui + 1 : ui); }
;         for (int t = 0; t < nt; t += 2) {
;             const bool last = (t == nt - 2);
;             const char* a1 = cA + (size_t)(t + 1) * kstep;
;             const char* a2 = last ? nA : cA + (size_t)(t + 2) * kstep; const char* b2 = last ? nB : cB + (size_t)(t + 2) * kstep;
;             const char* a3 = a2 + kstep; const char* b3 = b2 + kstep;
;             G8_LDB(B0, 0, 0); G8_LDB(B1, 0, 1); G8_SCHED; G8_LDA(At, 0, 0); G8_STGA(G8_SA(1, 1), 1, false, a1, (t + 1) * 128);
.LBB0_719:
	s_and_b64 s[6:7], s[82:83], exec
	s_cselect_b32 s13, s77, s65
	s_cselect_b32 s20, s76, s64
	s_cselect_b32 s21, s79, s17
	s_cselect_b32 s24, s78, s16
	s_add_u32 s2, s16, 0x100
	s_addc_u32 s12, s17, 0
	s_add_u32 s6, s64, 0x80
	s_addc_u32 s7, s65, 0
	v_ashrrev_i32_e32 v213, 31, v212
	s_waitcnt lgkmcnt(0)
	v_lshl_add_u64 v[2:3], s[6:7], 0, v[200:201]
	v_lshl_add_u64 v[218:219], v[2:3], 0, v[212:213]
	v_lshl_add_u64 v[2:3], s[6:7], 0, v[216:217]
	v_lshl_add_u64 v[220:221], v[2:3], 0, v[212:213]
	s_mov_b32 s25, 0
	s_mov_b64 s[16:17], 0
	s_branch .Lf8z_first
.Lf8z_first:
	v_add_u32_e32 v2, 0x10000, v237
	v_add_u32_e32 v6, 0x14000, v237
	ds_read_b128 v[26:29], v2
	ds_read_b128 v[30:33], v2 offset:1024
	ds_read_b128 v[18:21], v2 offset:2048
	ds_read_b128 v[22:25], v2 offset:3072
	ds_read_b128 v[10:13], v6
	ds_read_b128 v[14:17], v6 offset:1024
	ds_read_b128 v[2:5], v6 offset:2048
	ds_read_b128 v[6:9], v6 offset:3072
	ds_read_b128 v[58:61], v250
	ds_read_b128 v[62:65], v250 offset:1024
	ds_read_b128 v[50:53], v250 offset:2048
	ds_read_b128 v[54:57], v250 offset:3072
	ds_read_b128 v[42:45], v250 offset:4096
	ds_read_b128 v[46:49], v250 offset:5120
	ds_read_b128 v[34:37], v250 offset:6144
	ds_read_b128 v[38:41], v250 offset:7168
	s_and_b64 vcc, exec, s[40:41]
	s_mov_b64 s[6:7], -1
	s_cbranch_vccnz .Lf8z_723
	v_add_u32_e32 v66, s16, v206
	v_add_u32_e32 v66, 0x80, v66
	s_add_i32 m0, s0, 0xc000
	s_mov_b64 s[6:7], 0
	global_load_lds_dwordx4 v66, s[46:47]
	v_add_u32_e32 v66, s16, v204
	v_add_u32_e32 v66, 0x80, v66
	v_lshl_add_u64 v[222:223], s[46:47], 0, v[66:67]

; #define G8_STAGE(bufoff, gbase, voff) do { _Pragma("unroll") for (int _i = 0; _i < 2; ++_i) \
;         __builtin_amdgcn_global_load_lds((const unsigned*)((const char*)(gbase) + (voff)[_i]), (LAS unsigned*)(lds + (bufoff) + ldsw + _i * 8192), 16, 0, 0); } while (0)
; #define G8_LDA(dst, b, h) do { _Pragma("unroll") for (int m = 0; m < 4; ++m) _Pragma("unroll") for (int k = 0; k < 2; ++k) dst[m][k] = *(const LAS i32x4*)(lds + G8_SA(b, h) + aoff + m * 2048 + k * 1024); } while (0)
; #define G8_LDB(dst, b, h) do { _Pragma("unroll") for (int n = 0; n < 2; ++n) _Pragma("unroll") for (int k = 0; k < 2; ++k) dst[n][k] = *(const LAS i32x4*)(lds + G8_SB(b, h) + boff + n * 2048 + k * 1024); } while (0)
; #define G8_WAIT_V(n) asm volatile("s_waitcnt vmcnt(" #n ")" ::: "memory")
; #define G8_WAIT_L(n) asm volatile("s_waitcnt lgkmcnt(" #n ")" ::: "memory")
; #define G8_BAR __builtin_amdgcn_s_barrier()
; #define G8_SCHED __builtin_amdgcn_sched_barrier(0)
; template <bool FP8>
; __device__ __forceinline__ void gemm_phase(LAS unsigned char* lds, const Desc& prob) {
;     ...
;             const char* a2 = last ? nA : cA + (size_t)(t + 2) * kstep; const char* b2 = last ? nB : cB + (size_t)(t + 2) * kstep;
;             const char* a3 = a2 + kstep; const char* b3 = b2 + kstep;
;             G8_LDB(B0, 0, 0); G8_LDB(B1, 0, 1); G8_SCHED; G8_LDA(At, 0, 0); G8_STGA(G8_SA(1, 1), 1, false, a1, (t + 1) * 128);
;             G8_WAIT_V(8); G8_WAIT_L(0); G8_BAR; G8_MMA(0, 0, At, B0); G8_MMA(0, 1, At, B1); G8_BAR; G8_SCHED;
;             G8_LDA(At, 0, 1); G8_STAGE(G8_SB(0, 0), b2, voffB); G8_STAGE(G8_SB(0, 1), b2 + hstepB, voffB); G8_STGA(G8_SA(0, 0), 0, last, a2, last ? 0 : (t + 2) * 128);
;             G8_WAIT_V(8); G8_WAIT_L(0); G8_BAR; G8_MMA(1, 0, At, B0); G8_MMA(1, 1, At, B1); G8_BAR; G8_SCHED;
.Lf8z_725:
	s_cmp_eq_u32 s94, s25
	s_cselect_b64 s[42:43], -1, 0
	s_add_u32 s6, s64, s16
	s_addc_u32 s7, s65, s17
	s_add_u32 s8, s6, 0x100
	s_addc_u32 s9, s7, 0
	s_and_b64 s[6:7], s[42:43], exec
	s_cselect_b32 s7, s13, s9
	s_cselect_b32 s6, s20, s8
	s_add_u32 s73, s2, s16
	s_addc_u32 s75, s12, s17
	s_and_b64 s[8:9], s[42:43], exec
	s_cselect_b32 s9, s21, s75
	s_cselect_b32 s8, s24, s73
	s_add_i32 m0, s0, 0xe000
	s_nop 0
	global_load_lds_dwordx4 v[222:223], off
	s_waitcnt vmcnt(8)
	s_waitcnt lgkmcnt(0)
	s_barrier
	s_setprio 1
	s_waitcnt lgkmcnt(0)
	s_nop 1
	v_mfma_scale_f32_16x16x128_f8f6f4 v[72:75], v[26:33], v[58:65], 0, v1, v205 op_sel_hi:[0,0,0]
	s_nop 1
	v_mfma_scale_f32_16x16x128_f8f6f4 v[192:195], v[18:25], v[58:65], 0, v1, v205 op_sel_hi:[0,0,0]
	s_nop 1
	v_mfma_scale_f32_16x16x128_f8f6f4 v[188:191], v[26:33], v[50:57], 0, v1, v205 op_sel_hi:[0,0,0]
	s_nop 1
	v_mfma_scale_f32_16x16x128_f8f6f4 v[184:187], v[18:25], v[50:57], 0, v1, v205 op_sel_hi:[0,0,0]
	s_nop 1
	v_mfma_scale_f32_16x16x128_f8f6f4 v[180:183], v[26:33], v[42:49], 0, v1, v205 op_sel_hi:[0,0,0]
	s_nop 1
	v_mfma_scale_f32_16x16x128_f8f6f4 v[176:179], v[18:25], v[42:49], 0, v1, v205 op_sel_hi:[0,0,0]
	s_nop 1
	v_mfma_scale_f32_16x16x128_f8f6f4 v[172:175], v[26:33], v[34:41], 0, v1, v205 op_sel_hi:[0,0,0]
	s_nop 1
	v_mfma_scale_f32_16x16x128_f8f6f4 v[168:171], v[18:25], v[34:41], 0, v1, v205 op_sel_hi:[0,0,0]
	s_setprio 0
	s_setprio 1
	s_nop 1
	v_mfma_scale_f32_16x16x128_f8f6f4 v[164:167], v[10:17], v[58:65], 0, v1, v205 op_sel_hi:[0,0,0]
	s_nop 1
	v_mfma_scale_f32_16x16x128_f8f6f4 v[160:163], v[2:9], v[58:65], 0, v1, v205 op_sel_hi:[0,0,0]
	s_nop 1
	v_mfma_scale_f32_16x16x128_f8f6f4 v[156:159], v[10:17], v[50:57], 0, v1, v205 op_sel_hi:[0,0,0]
	s_nop 1
	v_mfma_scale_f32_16x16x128_f8f6f4 v[152:155], v[2:9], v[50:57], 0, v1, v205 op_sel_hi:[0,0,0]
	s_nop 1
	v_mfma_scale_f32_16x16x128_f8f6f4 v[148:151], v[10:17], v[42:49], 0, v1, v205 op_sel_hi:[0,0,0]
	s_nop 1
	v_mfma_scale_f32_16x16x128_f8f6f4 v[144:147], v[2:9], v[42:49], 0, v1, v205 op_sel_hi:[0,0,0]
	s_nop 1
	v_mfma_scale_f32_16x16x128_f8f6f4 v[140:143], v[10:17], v[34:41], 0, v1, v205 op_sel_hi:[0,0,0]
	s_nop 1
	v_mfma_scale_f32_16x16x128_f8f6f4 v[136:139], v[2:9], v[34:41], 0, v1, v205 op_sel_hi:[0,0,0]
	s_setprio 0
	s_barrier
	s_mov_b32 m0, s37
	v_lshl_add_u64 v[222:223], s[8:9], 0, v[208:209]
	v_lshl_add_u64 v[224:225], s[8:9], 0, v[210:211]
	s_add_u32 s8, s8, s62
	ds_read_b128 v[58:61], v250 offset:16384
	ds_read_b128 v[62:65], v250 offset:17408
	ds_read_b128 v[50:53], v250 offset:18432
	ds_read_b128 v[54:57], v250 offset:19456
	ds_read_b128 v[42:45], v250 offset:20480
	ds_read_b128 v[46:49], v250 offset:21504
	ds_read_b128 v[34:37], v250 offset:22528
	ds_read_b128 v[38:41], v250 offset:23552
	global_load_lds_dwordx4 v[222:223], off
	s_mov_b32 m0, s45
	s_addc_u32 s9, s9, s63
	global_load_lds_dwordx4 v[224:225], off
	v_lshl_add_u64 v[228:229], s[8:9], 0, v[208:209]
	s_mov_b32 m0, s59
	v_lshl_add_u64 v[230:231], s[8:9], 0, v[210:211]
	global_load_lds_dwordx4 v[228:229], off
	s_mov_b32 m0, s60
	s_mov_b64 s[8:9], -1
	global_load_lds_dwordx4 v[230:231], off
	s_and_b64 vcc, exec, s[10:11]
	v_cndmask_b32_e64 v243, v247, v249, s[42:43]
	v_cndmask_b32_e64 v213, v197, v239, s[42:43]
	s_cbranch_vccz .Lf8z_727
	s_add_i32 s73, s16, 0x100
	s_and_b64 s[8:9], s[42:43], exec
	s_cselect_b32 s8, 0, s73
	s_mov_b32 m0, s0
	v_add_u32_e32 v66, s8, v243
	global_load_lds_dwordx4 v66, s[46:47]
	v_add_u32_e32 v66, s8, v213
	v_lshl_add_u64 v[234:235], s[46:47], 0, v[66:67]
	s_mov_b64 s[8:9], 0

; #define G8_STAGE(bufoff, gbase, voff) do { _Pragma("unroll") for (int _i = 0; _i < 2; ++_i) \
;         __builtin_amdgcn_global_load_lds((const unsigned*)((const char*)(gbase) + (voff)[_i]), (LAS unsigned*)(lds + (bufoff) + ldsw + _i * 8192), 16, 0, 0); } while (0)
; #define G8_LDA(dst, b, h) do { _Pragma("unroll") for (int m = 0; m < 4; ++m) _Pragma("unroll") for (int k = 0; k < 2; ++k) dst[m][k] = *(const LAS i32x4*)(lds + G8_SA(b, h) + aoff + m * 2048 + k * 1024); } while (0)
; #define G8_WAIT_V(n) asm volatile("s_waitcnt vmcnt(" #n ")" ::: "memory")
; #define G8_WAIT_L(n) asm volatile("s_waitcnt lgkmcnt(" #n ")" ::: "memory")
; #define G8_BAR __builtin_amdgcn_s_barrier()
; #define G8_SCHED __builtin_amdgcn_sched_barrier(0)
; template <bool FP8>
; __device__ __forceinline__ void gemm_phase(LAS unsigned char* lds, const Desc& prob) {
;     ...
;             G8_WAIT_V(8); G8_WAIT_L(0); G8_BAR; G8_MMA(0, 0, At, B0); G8_MMA(0, 1, At, B1); G8_BAR; G8_SCHED;
;             G8_LDA(At, 0, 1); G8_STAGE(G8_SB(0, 0), b2, voffB); G8_STAGE(G8_SB(0, 1), b2 + hstepB, voffB); G8_STGA(G8_SA(0, 0), 0, last, a2, last ? 0 : (t + 2) * 128);
;             G8_WAIT_V(8); G8_WAIT_L(0); G8_BAR; G8_MMA(1, 0, At, B0); G8_MMA(1, 1, At, B1); G8_BAR; G8_SCHED;
.Lf8z_729:
	s_mov_b32 m0, s61
	s_nop 0
	global_load_lds_dwordx4 v[234:235], off
	s_waitcnt vmcnt(8)
	s_waitcnt lgkmcnt(0)
	s_barrier
	s_setprio 1
	s_waitcnt lgkmcnt(0)
	s_nop 1
	v_mfma_scale_f32_16x16x128_f8f6f4 v[132:135], v[26:33], v[58:65], 0, v1, v205 op_sel_hi:[0,0,0]
	s_nop 1
	v_mfma_scale_f32_16x16x128_f8f6f4 v[128:131], v[18:25], v[58:65], 0, v1, v205 op_sel_hi:[0,0,0]
	s_nop 1
	v_mfma_scale_f32_16x16x128_f8f6f4 v[124:127], v[26:33], v[50:57], 0, v1, v205 op_sel_hi:[0,0,0]
	s_nop 1
	v_mfma_scale_f32_16x16x128_f8f6f4 v[120:123], v[18:25], v[50:57], 0, v1, v205 op_sel_hi:[0,0,0]
	s_nop 1
	v_mfma_scale_f32_16x16x128_f8f6f4 v[116:119], v[26:33], v[42:49], 0, v1, v205 op_sel_hi:[0,0,0]
	s_nop 1
	v_mfma_scale_f32_16x16x128_f8f6f4 v[112:115], v[18:25], v[42:49], 0, v1, v205 op_sel_hi:[0,0,0]
	s_nop 1
	v_mfma_scale_f32_16x16x128_f8f6f4 v[108:111], v[26:33], v[34:41], 0, v1, v205 op_sel_hi:[0,0,0]
	s_nop 1
	v_mfma_scale_f32_16x16x128_f8f6f4 v[104:107], v[18:25], v[34:41], 0, v1, v205 op_sel_hi:[0,0,0]
	s_setprio 0
	s_setprio 1
	s_nop 1
	v_mfma_scale_f32_16x16x128_f8f6f4 v[100:103], v[10:17], v[58:65], 0, v1, v205 op_sel_hi:[0,0,0]
	s_nop 1
	v_mfma_scale_f32_16x16x128_f8f6f4 v[96:99], v[2:9], v[58:65], 0, v1, v205 op_sel_hi:[0,0,0]
	s_nop 1
	v_mfma_scale_f32_16x16x128_f8f6f4 v[92:95], v[10:17], v[50:57], 0, v1, v205 op_sel_hi:[0,0,0]
	s_nop 1
	v_mfma_scale_f32_16x16x128_f8f6f4 v[88:91], v[2:9], v[50:57], 0, v1, v205 op_sel_hi:[0,0,0]
	s_nop 1
	v_mfma_scale_f32_16x16x128_f8f6f4 v[84:87], v[10:17], v[42:49], 0, v1, v205 op_sel_hi:[0,0,0]
	s_nop 1
	v_mfma_scale_f32_16x16x128_f8f6f4 v[80:83], v[2:9], v[42:49], 0, v1, v205 op_sel_hi:[0,0,0]
	s_nop 1
	v_mfma_scale_f32_16x16x128_f8f6f4 v[76:79], v[10:17], v[34:41], 0, v1, v205 op_sel_hi:[0,0,0]
	s_nop 1
	v_mfma_scale_f32_16x16x128_f8f6f4 v[68:71], v[2:9], v[34:41], 0, v1, v205 op_sel_hi:[0,0,0]
	s_setprio 0
	s_barrier
	s_branch .Lf8z_mid

; #define G8_LDA(dst, b, h) do { _Pragma("unroll") for (int m = 0; m < 4; ++m) _Pragma("unroll") for (int k = 0; k < 2; ++k) dst[m][k] = *(const LAS i32x4*)(lds + G8_SA(b, h) + aoff + m * 2048 + k * 1024); } while (0)
; #define G8_LDB(dst, b, h) do { _Pragma("unroll") for (int n = 0; n < 2; ++n) _Pragma("unroll") for (int k = 0; k < 2; ++k) dst[n][k] = *(const LAS i32x4*)(lds + G8_SB(b, h) + boff + n * 2048 + k * 1024); } while (0)
; #define G8_SCHED __builtin_amdgcn_sched_barrier(0)
; template <bool FP8>
; __device__ __forceinline__ void gemm_phase(LAS unsigned char* lds, const Desc& prob) {
;     ...
;             G8_LDB(B0, 1, 0); G8_LDB(B1, 1, 1); G8_SCHED; G8_LDA(At, 1, 0); G8_STGA(G8_SA(0, 1), 1, last, a2, last ? 0 : (t + 2) * 128);
.Lf8z_mid:
	v_add_u32_e32 v2, 0x18000, v237
	v_add_u32_e32 v6, 0x1c000, v237
	ds_read_b128 v[26:29], v2
	ds_read_b128 v[30:33], v2 offset:1024
	ds_read_b128 v[18:21], v2 offset:2048
	ds_read_b128 v[22:25], v2 offset:3072
	ds_read_b128 v[10:13], v6
	ds_read_b128 v[14:17], v6 offset:1024
	ds_read_b128 v[2:5], v6 offset:2048
	ds_read_b128 v[6:9], v6 offset:3072
	ds_read_b128 v[58:61], v250 offset:32768
	ds_read_b128 v[62:65], v250 offset:33792
	ds_read_b128 v[50:53], v250 offset:34816
	ds_read_b128 v[54:57], v250 offset:35840
	ds_read_b128 v[42:45], v250 offset:36864
	ds_read_b128 v[46:49], v250 offset:37888
	ds_read_b128 v[34:37], v250 offset:38912
	ds_read_b128 v[38:41], v250 offset:39936
	s_and_b64 vcc, exec, s[40:41]
	s_mov_b64 s[8:9], -1
	s_cbranch_vccnz .LBB0_731
	s_add_i32 s73, s16, 0x100
	s_and_b64 s[8:9], s[42:43], exec
	s_cselect_b32 s8, 0, s73
	v_cndmask_b32_e64 v66, v206, v252, s[42:43]
	s_mov_b32 m0, s84
	v_add_u32_e32 v66, s8, v66
	global_load_lds_dwordx4 v66, s[46:47]
	v_cndmask_b32_e64 v66, v204, v241, s[42:43]
	v_add_u32_e32 v66, s8, v66
	v_lshl_add_u64 v[234:235], s[46:47], 0, v[66:67]
	s_mov_b64 s[8:9], 0
